# stack: attention dwordx4 stores via permlane32_swap + counted lgkmcnt in GEMM MFMA phases + back-edge rotation, on top of v31
# speedup vs baseline: 1.0076x; 1.0076x over previous
.LBB3_34:
	s_mov_b32 m0, s66
	ds_read_b128 v[98:101], v94 offset:16384
	ds_read_b128 v[102:105], v94 offset:17408
	ds_read_b128 v[106:109], v94 offset:18432
	ds_read_b128 v[110:113], v94 offset:19456
	ds_read_b128 v[114:117], v95
	ds_read_b128 v[118:121], v95 offset:1024
	ds_read_b128 v[122:125], v95 offset:2048
	ds_read_b128 v[126:129], v95 offset:3072
	ds_read_b128 v[130:133], v95 offset:4096
	ds_read_b128 v[134:137], v95 offset:5120
	ds_read_b128 v[138:141], v95 offset:6144
	ds_read_b128 v[142:145], v95 offset:7168
	global_load_lds_dwordx4 v[146:147], off
	v_lshl_add_u64 v[146:147], v[74:75], 0, s[24:25]
	s_add_i32 m0, s66, 0x2000
	s_nop 0
	global_load_lds_dwordx4 v[146:147], off
	s_barrier
	s_setprio 1
	s_waitcnt lgkmcnt(7)
	v_mfma_f32_16x16x32_f16 v[44:47], v[98:101], v[114:117], v[44:47]
	v_mfma_f32_16x16x32_f16 v[40:43], v[106:109], v[114:117], v[40:43]
	s_waitcnt lgkmcnt(5)
	v_mfma_f32_16x16x32_f16 v[32:35], v[98:101], v[122:125], v[32:35]
	v_mfma_f32_16x16x32_f16 v[28:31], v[106:109], v[122:125], v[28:31]
	s_waitcnt lgkmcnt(3)
	v_mfma_f32_16x16x32_f16 v[20:23], v[98:101], v[130:133], v[20:23]
	v_mfma_f32_16x16x32_f16 v[16:19], v[106:109], v[130:133], v[16:19]
	s_waitcnt lgkmcnt(1)
	v_mfma_f32_16x16x32_f16 v[8:11], v[98:101], v[138:141], v[8:11]
	v_mfma_f32_16x16x32_f16 v[4:7], v[106:109], v[138:141], v[4:7]
	v_mfma_f32_16x16x32_f16 v[44:47], v[102:105], v[118:121], v[44:47]
	v_mfma_f32_16x16x32_f16 v[40:43], v[110:113], v[118:121], v[40:43]
	v_mfma_f32_16x16x32_f16 v[32:35], v[102:105], v[126:129], v[32:35]
	v_mfma_f32_16x16x32_f16 v[28:31], v[110:113], v[126:129], v[28:31]
	v_mfma_f32_16x16x32_f16 v[20:23], v[102:105], v[134:137], v[20:23]
	v_mfma_f32_16x16x32_f16 v[16:19], v[110:113], v[134:137], v[16:19]
	s_waitcnt lgkmcnt(0)
	v_mfma_f32_16x16x32_f16 v[8:11], v[102:105], v[142:145], v[8:11]
	v_mfma_f32_16x16x32_f16 v[4:7], v[110:113], v[142:145], v[4:7]
	s_setprio 0
	s_barrier
	v_lshl_add_u64 v[106:107], v[76:77], 0, s[24:25]
	s_add_i32 m0, s43, 0x18000
	ds_read_b128 v[98:101], v94 offset:20480
	ds_read_b128 v[102:105], v94 offset:21504
	global_load_lds_dwordx4 v[106:107], off
	v_lshl_add_u64 v[106:107], v[78:79], 0, s[24:25]
	s_add_i32 m0, s43, 0x1a000
	s_nop 0
	global_load_lds_dwordx4 v[106:107], off
	v_lshl_add_u64 v[106:107], v[80:81], 0, s[24:25]
	s_add_i32 m0, s43, 0x1c000
	s_nop 0
	global_load_lds_dwordx4 v[106:107], off
	s_waitcnt vmcnt(5)
	s_barrier
	s_setprio 1
	s_waitcnt lgkmcnt(1)
	v_mfma_f32_16x16x32_f16 v[36:39], v[98:101], v[114:117], v[36:39]
	v_mfma_f32_16x16x32_f16 v[24:27], v[98:101], v[122:125], v[24:27]
	v_mfma_f32_16x16x32_f16 v[12:15], v[98:101], v[130:133], v[12:15]
	v_mfma_f32_16x16x32_f16 v[0:3], v[98:101], v[138:141], v[0:3]
	s_waitcnt lgkmcnt(0)
	v_mfma_f32_16x16x32_f16 v[36:39], v[102:105], v[118:121], v[36:39]
	v_mfma_f32_16x16x32_f16 v[24:27], v[102:105], v[126:129], v[24:27]
	v_mfma_f32_16x16x32_f16 v[12:15], v[102:105], v[134:137], v[12:15]
	v_mfma_f32_16x16x32_f16 v[0:3], v[102:105], v[142:145], v[0:3]
	s_setprio 0
	s_barrier
	s_mov_b32 m0, s43
	v_lshl_add_u64 v[146:147], s[64:65], 0, v[48:49]
	ds_read_b128 v[98:101], v94 offset:57344
	ds_read_b128 v[102:105], v94 offset:58368
	ds_read_b128 v[106:109], v94 offset:59392
	ds_read_b128 v[110:113], v94 offset:60416
	ds_read_b128 v[114:117], v95 offset:40960
	ds_read_b128 v[118:121], v95 offset:41984
	ds_read_b128 v[122:125], v95 offset:43008
	ds_read_b128 v[126:129], v95 offset:44032
	ds_read_b128 v[130:133], v95 offset:45056
	ds_read_b128 v[134:137], v95 offset:46080
	ds_read_b128 v[138:141], v95 offset:47104
	ds_read_b128 v[142:145], v95 offset:48128
	global_load_lds_dwordx4 v[146:147], off
	v_lshl_add_u64 v[148:149], s[64:65], 0, v[52:53]
	s_mov_b32 m0, s44
	s_nop 0
	global_load_lds_dwordx4 v[148:149], off
	s_barrier
	s_setprio 1
	s_waitcnt lgkmcnt(7)
	v_mfma_f32_16x16x32_f16 v[44:47], v[98:101], v[114:117], v[44:47]
	v_mfma_f32_16x16x32_f16 v[40:43], v[106:109], v[114:117], v[40:43]
	s_waitcnt lgkmcnt(5)
	v_mfma_f32_16x16x32_f16 v[32:35], v[98:101], v[122:125], v[32:35]
	v_mfma_f32_16x16x32_f16 v[28:31], v[106:109], v[122:125], v[28:31]
	s_waitcnt lgkmcnt(3)
	v_mfma_f32_16x16x32_f16 v[20:23], v[98:101], v[130:133], v[20:23]
	v_mfma_f32_16x16x32_f16 v[16:19], v[106:109], v[130:133], v[16:19]
	s_waitcnt lgkmcnt(1)
	v_mfma_f32_16x16x32_f16 v[8:11], v[98:101], v[138:141], v[8:11]
	v_mfma_f32_16x16x32_f16 v[4:7], v[106:109], v[138:141], v[4:7]
	v_mfma_f32_16x16x32_f16 v[44:47], v[102:105], v[118:121], v[44:47]
	v_mfma_f32_16x16x32_f16 v[40:43], v[110:113], v[118:121], v[40:43]
	v_mfma_f32_16x16x32_f16 v[32:35], v[102:105], v[126:129], v[32:35]
	v_mfma_f32_16x16x32_f16 v[28:31], v[110:113], v[126:129], v[28:31]
	v_mfma_f32_16x16x32_f16 v[20:23], v[102:105], v[134:137], v[20:23]
	v_mfma_f32_16x16x32_f16 v[16:19], v[110:113], v[134:137], v[16:19]
	s_waitcnt lgkmcnt(0)
	v_mfma_f32_16x16x32_f16 v[8:11], v[102:105], v[142:145], v[8:11]
	v_mfma_f32_16x16x32_f16 v[4:7], v[110:113], v[142:145], v[4:7]
	s_setprio 0
	s_barrier
	s_mov_b32 m0, s45
	v_lshl_add_u64 v[150:151], s[26:27], 0, v[50:51]
	ds_read_b128 v[98:101], v94 offset:61440
	ds_read_b128 v[102:105], v94 offset:62464
	global_load_lds_dwordx4 v[150:151], off
	v_lshl_add_u64 v[152:153], s[26:27], 0, v[54:55]
	s_mov_b32 m0, s46
	v_lshl_add_u64 v[154:155], s[26:27], 0, v[56:57]
	global_load_lds_dwordx4 v[152:153], off
	s_mov_b32 m0, s47
	s_nop 0
	global_load_lds_dwordx4 v[154:155], off
	s_waitcnt vmcnt(5)
	s_barrier
	s_setprio 1
	s_waitcnt lgkmcnt(1)
	v_mfma_f32_16x16x32_f16 v[36:39], v[98:101], v[114:117], v[36:39]
	v_mfma_f32_16x16x32_f16 v[24:27], v[98:101], v[122:125], v[24:27]
	v_mfma_f32_16x16x32_f16 v[12:15], v[98:101], v[130:133], v[12:15]
	v_mfma_f32_16x16x32_f16 v[0:3], v[98:101], v[138:141], v[0:3]
	s_waitcnt lgkmcnt(0)
	v_mfma_f32_16x16x32_f16 v[36:39], v[102:105], v[118:121], v[36:39]
	v_mfma_f32_16x16x32_f16 v[24:27], v[102:105], v[126:129], v[24:27]
	v_mfma_f32_16x16x32_f16 v[12:15], v[102:105], v[134:137], v[12:15]
	v_mfma_f32_16x16x32_f16 v[0:3], v[102:105], v[142:145], v[0:3]
	s_setprio 0
	s_barrier
	s_mov_b32 m0, s52
	v_lshl_add_u64 v[146:147], v[146:147], 0, s[16:17]
	ds_read_b128 v[98:101], v96
	ds_read_b128 v[102:105], v96 offset:1024
	ds_read_b128 v[106:109], v96 offset:2048
	ds_read_b128 v[110:113], v96 offset:3072
	ds_read_b128 v[114:117], v97
	ds_read_b128 v[118:121], v97 offset:1024
	ds_read_b128 v[122:125], v97 offset:2048
	ds_read_b128 v[126:129], v97 offset:3072
	ds_read_b128 v[130:133], v97 offset:4096
	ds_read_b128 v[134:137], v97 offset:5120
	ds_read_b128 v[138:141], v97 offset:6144
	ds_read_b128 v[142:145], v97 offset:7168
	global_load_lds_dwordx4 v[146:147], off
	v_lshl_add_u64 v[146:147], v[148:149], 0, s[16:17]
	s_mov_b32 m0, s53
	s_nop 0
	global_load_lds_dwordx4 v[146:147], off
	s_barrier
	s_setprio 1
	s_waitcnt lgkmcnt(7)
	v_mfma_f32_16x16x32_f16 v[44:47], v[98:101], v[114:117], v[44:47]
	v_mfma_f32_16x16x32_f16 v[40:43], v[106:109], v[114:117], v[40:43]
	s_waitcnt lgkmcnt(5)
	v_mfma_f32_16x16x32_f16 v[32:35], v[98:101], v[122:125], v[32:35]
	v_mfma_f32_16x16x32_f16 v[28:31], v[106:109], v[122:125], v[28:31]
	s_waitcnt lgkmcnt(3)
	v_mfma_f32_16x16x32_f16 v[20:23], v[98:101], v[130:133], v[20:23]
	v_mfma_f32_16x16x32_f16 v[16:19], v[106:109], v[130:133], v[16:19]
	s_waitcnt lgkmcnt(1)
	v_mfma_f32_16x16x32_f16 v[8:11], v[98:101], v[138:141], v[8:11]
	v_mfma_f32_16x16x32_f16 v[4:7], v[106:109], v[138:141], v[4:7]
	v_mfma_f32_16x16x32_f16 v[44:47], v[102:105], v[118:121], v[44:47]
	v_mfma_f32_16x16x32_f16 v[40:43], v[110:113], v[118:121], v[40:43]
	v_mfma_f32_16x16x32_f16 v[32:35], v[102:105], v[126:129], v[32:35]
	v_mfma_f32_16x16x32_f16 v[28:31], v[110:113], v[126:129], v[28:31]
	v_mfma_f32_16x16x32_f16 v[20:23], v[102:105], v[134:137], v[20:23]
	v_mfma_f32_16x16x32_f16 v[16:19], v[110:113], v[134:137], v[16:19]
	s_waitcnt lgkmcnt(0)
	v_mfma_f32_16x16x32_f16 v[8:11], v[102:105], v[142:145], v[8:11]
	v_mfma_f32_16x16x32_f16 v[4:7], v[110:113], v[142:145], v[4:7]
	s_setprio 0
	s_barrier
	s_mov_b32 m0, s54
	v_lshl_add_u64 v[106:107], v[150:151], 0, s[16:17]
	ds_read_b128 v[98:101], v96 offset:4096
	ds_read_b128 v[102:105], v96 offset:5120
	global_load_lds_dwordx4 v[106:107], off
	v_lshl_add_u64 v[106:107], v[152:153], 0, s[16:17]
	s_add_i32 m0, s54, 0x2000
	s_nop 0
	global_load_lds_dwordx4 v[106:107], off
	v_lshl_add_u64 v[106:107], v[154:155], 0, s[16:17]
	s_add_i32 m0, s54, 0x4000
	s_nop 0
	global_load_lds_dwordx4 v[106:107], off
	s_waitcnt vmcnt(5)
	s_barrier
	s_setprio 1
	s_waitcnt lgkmcnt(1)
	v_mfma_f32_16x16x32_f16 v[36:39], v[98:101], v[114:117], v[36:39]
	v_mfma_f32_16x16x32_f16 v[24:27], v[98:101], v[122:125], v[24:27]
	v_mfma_f32_16x16x32_f16 v[12:15], v[98:101], v[130:133], v[12:15]
	v_mfma_f32_16x16x32_f16 v[0:3], v[98:101], v[138:141], v[0:3]
	s_waitcnt lgkmcnt(0)
	v_mfma_f32_16x16x32_f16 v[36:39], v[102:105], v[118:121], v[36:39]
	v_mfma_f32_16x16x32_f16 v[24:27], v[102:105], v[126:129], v[24:27]
	v_mfma_f32_16x16x32_f16 v[12:15], v[102:105], v[134:137], v[12:15]
	v_mfma_f32_16x16x32_f16 v[0:3], v[102:105], v[142:145], v[0:3]
	s_setprio 0
	s_add_i32 s63, s63, 3
	s_add_u32 s24, s24, 0x180
	s_addc_u32 s25, s25, 0
	s_cmp_ge_i32 s63, s49
	s_cbranch_scc1 .Lrot_exit_qkv
	s_add_u32 s26, s20, s24
	s_addc_u32 s27, s21, s25
	s_add_u32 s26, s26, 0x180
	s_addc_u32 s27, s27, 0
	s_add_u32 s64, s22, s24
	s_addc_u32 s65, s23, s25
	s_add_u32 s66, s64, 0x180
	s_addc_u32 s67, s65, 0
	s_cmp_eq_u32 s56, s63
	s_cselect_b32 s65, s5, s27
	s_cselect_b32 s64, s4, s26
	s_cselect_b32 s27, s7, s67
	s_cselect_b32 s26, s6, s66
	s_add_i32 s66, s58, s38
	v_lshl_add_u64 v[146:147], v[72:73], 0, s[24:25]
	s_barrier
	s_branch .LBB3_34

.LBB4_22:
	s_mov_b32 m0, s70
	ds_read_b128 v[130:133], v136 offset:16384
	ds_read_b128 v[142:145], v136 offset:17408
	ds_read_b128 v[146:149], v136 offset:18432
	ds_read_b128 v[150:153], v136 offset:19456
	ds_read_b128 v[154:157], v137
	ds_read_b128 v[158:161], v137 offset:1024
	ds_read_b128 v[162:165], v137 offset:2048
	ds_read_b128 v[166:169], v137 offset:3072
	ds_read_b128 v[170:173], v137 offset:4096
	ds_read_b128 v[174:177], v137 offset:5120
	ds_read_b128 v[178:181], v137 offset:6144
	ds_read_b128 v[182:185], v137 offset:7168
	global_load_lds_dwordx4 v[108:109], off
	v_lshl_add_u64 v[108:109], v[100:101], 0, s[30:31]
	s_add_i32 m0, s70, 0x2000
	s_nop 0
	global_load_lds_dwordx4 v[108:109], off
	s_barrier
	s_setprio 1
	s_waitcnt lgkmcnt(7)
	v_mfma_f32_16x16x32_f16 v[94:97], v[130:133], v[154:157], v[94:97]
	v_mfma_f32_16x16x32_f16 v[90:93], v[146:149], v[154:157], v[90:93]
	s_waitcnt lgkmcnt(5)
	v_mfma_f32_16x16x32_f16 v[82:85], v[130:133], v[162:165], v[82:85]
	v_mfma_f32_16x16x32_f16 v[78:81], v[146:149], v[162:165], v[78:81]
	s_waitcnt lgkmcnt(3)
	v_mfma_f32_16x16x32_f16 v[70:73], v[130:133], v[170:173], v[70:73]
	v_mfma_f32_16x16x32_f16 v[66:69], v[146:149], v[170:173], v[66:69]
	s_waitcnt lgkmcnt(1)
	v_mfma_f32_16x16x32_f16 v[58:61], v[130:133], v[178:181], v[58:61]
	v_mfma_f32_16x16x32_f16 v[54:57], v[146:149], v[178:181], v[54:57]
	v_mfma_f32_16x16x32_f16 v[94:97], v[142:145], v[158:161], v[94:97]
	v_mfma_f32_16x16x32_f16 v[90:93], v[150:153], v[158:161], v[90:93]
	v_mfma_f32_16x16x32_f16 v[82:85], v[142:145], v[166:169], v[82:85]
	v_mfma_f32_16x16x32_f16 v[78:81], v[150:153], v[166:169], v[78:81]
	v_mfma_f32_16x16x32_f16 v[70:73], v[142:145], v[174:177], v[70:73]
	v_mfma_f32_16x16x32_f16 v[66:69], v[150:153], v[174:177], v[66:69]
	s_waitcnt lgkmcnt(0)
	v_mfma_f32_16x16x32_f16 v[58:61], v[142:145], v[182:185], v[58:61]
	v_mfma_f32_16x16x32_f16 v[54:57], v[150:153], v[182:185], v[54:57]
	s_setprio 0
	s_barrier
	v_lshl_add_u64 v[108:109], v[102:103], 0, s[30:31]
	s_add_i32 m0, s49, 0x18000
	ds_read_b128 v[130:133], v136 offset:20480
	ds_read_b128 v[142:145], v136 offset:21504
	global_load_lds_dwordx4 v[108:109], off
	v_lshl_add_u64 v[108:109], v[104:105], 0, s[30:31]
	s_add_i32 m0, s49, 0x1a000
	s_nop 0
	global_load_lds_dwordx4 v[108:109], off
	v_lshl_add_u64 v[108:109], v[106:107], 0, s[30:31]
	s_add_i32 m0, s49, 0x1c000
	s_nop 0
	global_load_lds_dwordx4 v[108:109], off
	s_cmp_lg_u32 s67, 0
	s_cbranch_scc1 .Lpj_norm_0
	s_mul_i32 s72, s66, 0xc0
	v_add_u32_e32 v214, s72, v135
	v_ashrrev_i32_e32 v215, 31, v214
	v_lshl_add_u64 v[214:215], v[214:215], 2, s[10:11]
	global_load_dwordx4 v[202:205], v[214:215], off
	global_load_dwordx4 v[206:209], v[214:215], off offset:64
	global_load_dwordx4 v[210:213], v[214:215], off offset:128
	global_load_dwordx4 v[2:5], v[194:195], off
	global_load_dwordx4 v[6:9], v[194:195], off offset:64
	global_load_dwordx4 v[10:13], v[194:195], off offset:128
	global_load_dwordx4 v[14:17], v[196:197], off
	s_waitcnt vmcnt(12)
	s_branch .Lpj_join_0

.Lpj_join_2:
	s_barrier
	s_setprio 1
	s_waitcnt lgkmcnt(1)
	v_mfma_f32_16x16x32_f16 v[86:89], v[130:133], v[154:157], v[86:89]
	v_mfma_f32_16x16x32_f16 v[74:77], v[130:133], v[162:165], v[74:77]
	v_mfma_f32_16x16x32_f16 v[62:65], v[130:133], v[170:173], v[62:65]
	v_mfma_f32_16x16x32_f16 v[50:53], v[130:133], v[178:181], v[50:53]
	s_waitcnt lgkmcnt(0)
	v_mfma_f32_16x16x32_f16 v[86:89], v[142:145], v[158:161], v[86:89]
	v_mfma_f32_16x16x32_f16 v[74:77], v[142:145], v[166:169], v[74:77]
	v_mfma_f32_16x16x32_f16 v[62:65], v[142:145], v[174:177], v[62:65]
	v_mfma_f32_16x16x32_f16 v[50:53], v[142:145], v[182:185], v[50:53]
	s_setprio 0
	s_add_i32 s67, s67, 3
	s_add_u32 s30, s30, 0x180
	s_addc_u32 s31, s31, 0
	s_cmp_ge_i32 s67, s59
	s_cbranch_scc1 .Lrot_exit_proj
	s_add_u32 s34, s26, s30
	s_addc_u32 s35, s27, s31
	s_add_u32 s34, s34, 0x180
	s_addc_u32 s35, s35, 0
	s_add_u32 s68, s28, s30
	s_addc_u32 s69, s29, s31
	s_add_u32 s70, s68, 0x180
	s_addc_u32 s71, s69, 0
	s_cmp_eq_u32 s60, s67
	s_cselect_b32 s69, s5, s35
	s_cselect_b32 s68, s4, s34
	s_cselect_b32 s35, s7, s71
	s_cselect_b32 s34, s6, s70
	s_add_i32 s70, s62, s44
	v_lshl_add_u64 v[108:109], v[98:99], 0, s[30:31]
	s_barrier
	s_branch .LBB4_22

.LBB5_55:
	s_mov_b32 m0, s76
	ds_read_b128 v[44:47], v130 offset:16384
	ds_read_b128 v[56:59], v130 offset:17408
	ds_read_b128 v[60:63], v130 offset:18432
	ds_read_b128 v[64:67], v130 offset:19456
	ds_read_b128 v[68:71], v131
	ds_read_b128 v[96:99], v131 offset:1024
	ds_read_b128 v[136:139], v131 offset:2048
	ds_read_b128 v[140:143], v131 offset:3072
	ds_read_b128 v[144:147], v131 offset:4096
	ds_read_b128 v[148:151], v131 offset:5120
	ds_read_b128 v[152:155], v131 offset:6144
	ds_read_b128 v[156:159], v131 offset:7168
	global_load_lds_dwordx4 v[126:127], off
	v_lshl_add_u64 v[126:127], v[34:35], 0, s[44:45]
	s_add_i32 m0, s76, 0x2000
	s_add_i32 s76, s27, s54
	global_load_lds_dwordx4 v[126:127], off
	v_lshl_add_u64 v[126:127], v[36:37], 0, s[44:45]
	s_mov_b32 m0, s76
	s_nop 0
	global_load_lds_dwordx4 v[126:127], off
	v_lshl_add_u64 v[126:127], v[38:39], 0, s[44:45]
	s_add_i32 m0, s76, 0x2000
	s_nop 0
	global_load_lds_dwordx4 v[126:127], off
	s_barrier
	s_setprio 1
	s_waitcnt lgkmcnt(7)
	v_mfma_f32_16x16x32_f16 v[92:95], v[44:47], v[68:71], v[92:95]
	v_mfma_f32_16x16x32_f16 v[88:91], v[60:63], v[68:71], v[88:91]
	s_waitcnt lgkmcnt(5)
	v_mfma_f32_16x16x32_f16 v[76:79], v[44:47], v[136:139], v[76:79]
	v_mfma_f32_16x16x32_f16 v[72:75], v[60:63], v[136:139], v[72:75]
	s_waitcnt lgkmcnt(3)
	v_mfma_f32_16x16x32_f16 v[28:31], v[44:47], v[144:147], v[28:31]
	v_mfma_f32_16x16x32_f16 v[24:27], v[60:63], v[144:147], v[24:27]
	s_waitcnt lgkmcnt(1)
	v_mfma_f32_16x16x32_f16 v[12:15], v[44:47], v[152:155], v[12:15]
	v_mfma_f32_16x16x32_f16 v[8:11], v[60:63], v[152:155], v[8:11]
	v_mfma_f32_16x16x32_f16 v[92:95], v[56:59], v[96:99], v[92:95]
	v_mfma_f32_16x16x32_f16 v[88:91], v[64:67], v[96:99], v[88:91]
	v_mfma_f32_16x16x32_f16 v[76:79], v[56:59], v[140:143], v[76:79]
	v_mfma_f32_16x16x32_f16 v[72:75], v[64:67], v[140:143], v[72:75]
	v_mfma_f32_16x16x32_f16 v[28:31], v[56:59], v[148:151], v[28:31]
	v_mfma_f32_16x16x32_f16 v[24:27], v[64:67], v[148:151], v[24:27]
	s_waitcnt lgkmcnt(0)
	v_mfma_f32_16x16x32_f16 v[12:15], v[56:59], v[156:159], v[12:15]
	v_mfma_f32_16x16x32_f16 v[8:11], v[64:67], v[156:159], v[8:11]
	s_setprio 0
	s_barrier
	s_add_i32 s76, s68, s54
	v_lshl_add_u64 v[126:127], v[40:41], 0, s[44:45]
	s_mov_b32 m0, s76
	ds_read_b128 v[44:47], v130 offset:32768
	ds_read_b128 v[56:59], v130 offset:33792
	ds_read_b128 v[60:63], v130 offset:34816
	ds_read_b128 v[64:67], v130 offset:35840
	global_load_lds_dwordx4 v[126:127], off
	v_lshl_add_u64 v[126:127], v[42:43], 0, s[44:45]
	s_add_i32 m0, s76, 0x2000
	s_nop 0
	global_load_lds_dwordx4 v[126:127], off
	s_waitcnt vmcnt(6)
	s_barrier
	s_setprio 1
	s_waitcnt lgkmcnt(3)
	v_mfma_f32_16x16x32_f16 v[84:87], v[44:47], v[68:71], v[84:87]
	v_mfma_f32_16x16x32_f16 v[52:55], v[44:47], v[136:139], v[52:55]
	s_waitcnt lgkmcnt(1)
	v_mfma_f32_16x16x32_f16 v[48:51], v[60:63], v[136:139], v[48:51]
	v_mfma_f32_16x16x32_f16 v[20:23], v[44:47], v[144:147], v[20:23]
	v_mfma_f32_16x16x32_f16 v[16:19], v[60:63], v[144:147], v[16:19]
	v_mfma_f32_16x16x32_f16 v[4:7], v[44:47], v[152:155], v[4:7]
	v_mfma_f32_16x16x32_f16 v[0:3], v[60:63], v[152:155], v[0:3]
	v_mfma_f32_16x16x32_f16 v[84:87], v[56:59], v[96:99], v[84:87]
	v_mfma_f32_16x16x32_f16 v[68:71], v[60:63], v[68:71], v[80:83]
	v_mfma_f32_16x16x32_f16 v[52:55], v[56:59], v[140:143], v[52:55]
	s_waitcnt lgkmcnt(0)
	v_mfma_f32_16x16x32_f16 v[48:51], v[64:67], v[140:143], v[48:51]
	v_mfma_f32_16x16x32_f16 v[20:23], v[56:59], v[148:151], v[20:23]
	v_mfma_f32_16x16x32_f16 v[16:19], v[64:67], v[148:151], v[16:19]
	v_mfma_f32_16x16x32_f16 v[4:7], v[56:59], v[156:159], v[4:7]
	v_mfma_f32_16x16x32_f16 v[0:3], v[64:67], v[156:159], v[0:3]
	v_mfma_f32_16x16x32_f16 v[68:71], v[64:67], v[96:99], v[68:71]
	s_setprio 0
	s_barrier
	s_add_i32 s76, 0, 0x10000
	s_mov_b32 m0, s57
	v_add_u32_e32 v64, s76, v128
	v_lshl_add_u64 v[126:127], s[48:49], 0, v[100:101]
	ds_read_b128 v[44:47], v64
	ds_read_b128 v[56:59], v64 offset:1024
	ds_read_b128 v[60:63], v64 offset:2048
	ds_read_b128 v[64:67], v64 offset:3072
	ds_read_b128 v[80:83], v131 offset:49152
	ds_read_b128 v[96:99], v131 offset:50176
	ds_read_b128 v[136:139], v131 offset:51200
	ds_read_b128 v[140:143], v131 offset:52224
	ds_read_b128 v[144:147], v131 offset:53248
	ds_read_b128 v[148:151], v131 offset:54272
	ds_read_b128 v[152:155], v131 offset:55296
	ds_read_b128 v[156:159], v131 offset:56320
	global_load_lds_dwordx4 v[126:127], off
	v_lshl_add_u64 v[160:161], s[48:49], 0, v[104:105]
	s_mov_b32 m0, s58
	v_lshl_add_u64 v[162:163], s[46:47], 0, v[102:103]
	global_load_lds_dwordx4 v[160:161], off
	s_mov_b32 m0, s59
	v_lshl_add_u64 v[164:165], s[46:47], 0, v[106:107]
	global_load_lds_dwordx4 v[162:163], off
	s_mov_b32 m0, s60
	s_nop 0
	global_load_lds_dwordx4 v[164:165], off
	s_barrier
	s_setprio 1
	s_waitcnt lgkmcnt(7)
	v_mfma_f32_16x16x32_f16 v[92:95], v[44:47], v[80:83], v[92:95]
	v_mfma_f32_16x16x32_f16 v[88:91], v[60:63], v[80:83], v[88:91]
	s_waitcnt lgkmcnt(5)
	v_mfma_f32_16x16x32_f16 v[76:79], v[44:47], v[136:139], v[76:79]
	v_mfma_f32_16x16x32_f16 v[72:75], v[60:63], v[136:139], v[72:75]
	s_waitcnt lgkmcnt(3)
	v_mfma_f32_16x16x32_f16 v[28:31], v[44:47], v[144:147], v[28:31]
	v_mfma_f32_16x16x32_f16 v[24:27], v[60:63], v[144:147], v[24:27]
	s_waitcnt lgkmcnt(1)
	v_mfma_f32_16x16x32_f16 v[12:15], v[44:47], v[152:155], v[12:15]
	v_mfma_f32_16x16x32_f16 v[8:11], v[60:63], v[152:155], v[8:11]
	v_mfma_f32_16x16x32_f16 v[92:95], v[56:59], v[96:99], v[92:95]
	v_mfma_f32_16x16x32_f16 v[88:91], v[64:67], v[96:99], v[88:91]
	v_mfma_f32_16x16x32_f16 v[76:79], v[56:59], v[140:143], v[76:79]
	v_mfma_f32_16x16x32_f16 v[72:75], v[64:67], v[140:143], v[72:75]
	v_mfma_f32_16x16x32_f16 v[28:31], v[56:59], v[148:151], v[28:31]
	v_mfma_f32_16x16x32_f16 v[24:27], v[64:67], v[148:151], v[24:27]
	s_waitcnt lgkmcnt(0)
	v_mfma_f32_16x16x32_f16 v[12:15], v[56:59], v[156:159], v[12:15]
	v_mfma_f32_16x16x32_f16 v[8:11], v[64:67], v[156:159], v[8:11]
	s_setprio 0
	s_barrier
	s_add_i32 s48, 0, 0x14000
	s_add_u32 s46, s46, s10
	s_addc_u32 s47, s47, s11
	s_mov_b32 m0, s61
	v_add_u32_e32 v64, s48, v128
	v_lshl_add_u64 v[166:167], s[46:47], 0, v[102:103]
	ds_read_b128 v[44:47], v64
	ds_read_b128 v[56:59], v64 offset:1024
	ds_read_b128 v[60:63], v64 offset:2048
	ds_read_b128 v[64:67], v64 offset:3072
	global_load_lds_dwordx4 v[166:167], off
	v_lshl_add_u64 v[168:169], s[46:47], 0, v[106:107]
	s_mov_b32 m0, s62
	s_nop 0
	global_load_lds_dwordx4 v[168:169], off
	s_waitcnt vmcnt(6)
	s_barrier
	s_setprio 1
	s_waitcnt lgkmcnt(3)
	v_mfma_f32_16x16x32_f16 v[84:87], v[44:47], v[80:83], v[84:87]
	v_mfma_f32_16x16x32_f16 v[52:55], v[44:47], v[136:139], v[52:55]
	s_waitcnt lgkmcnt(1)
	v_mfma_f32_16x16x32_f16 v[48:51], v[60:63], v[136:139], v[48:51]
	v_mfma_f32_16x16x32_f16 v[20:23], v[44:47], v[144:147], v[20:23]
	v_mfma_f32_16x16x32_f16 v[16:19], v[60:63], v[144:147], v[16:19]
	v_mfma_f32_16x16x32_f16 v[4:7], v[44:47], v[152:155], v[4:7]
	v_mfma_f32_16x16x32_f16 v[0:3], v[60:63], v[152:155], v[0:3]
	v_mfma_f32_16x16x32_f16 v[84:87], v[56:59], v[96:99], v[84:87]
	v_mfma_f32_16x16x32_f16 v[68:71], v[60:63], v[80:83], v[68:71]
	v_mfma_f32_16x16x32_f16 v[52:55], v[56:59], v[140:143], v[52:55]
	s_waitcnt lgkmcnt(0)
	v_mfma_f32_16x16x32_f16 v[48:51], v[64:67], v[140:143], v[48:51]
	v_mfma_f32_16x16x32_f16 v[20:23], v[56:59], v[148:151], v[20:23]
	v_mfma_f32_16x16x32_f16 v[16:19], v[64:67], v[148:151], v[16:19]
	v_mfma_f32_16x16x32_f16 v[4:7], v[56:59], v[156:159], v[4:7]
	v_mfma_f32_16x16x32_f16 v[0:3], v[64:67], v[156:159], v[0:3]
	v_mfma_f32_16x16x32_f16 v[68:71], v[64:67], v[96:99], v[68:71]
	s_setprio 0
	s_barrier
	s_mov_b32 m0, s64
	v_lshl_add_u64 v[126:127], v[126:127], 0, s[22:23]
	ds_read_b128 v[44:47], v132
	ds_read_b128 v[56:59], v132 offset:1024
	ds_read_b128 v[60:63], v132 offset:2048
	ds_read_b128 v[64:67], v132 offset:3072
	ds_read_b128 v[80:83], v133
	ds_read_b128 v[96:99], v133 offset:1024
	ds_read_b128 v[136:139], v133 offset:2048
	ds_read_b128 v[140:143], v133 offset:3072
	ds_read_b128 v[144:147], v133 offset:4096
	ds_read_b128 v[148:151], v133 offset:5120
	ds_read_b128 v[152:155], v133 offset:6144
	ds_read_b128 v[156:159], v133 offset:7168
	global_load_lds_dwordx4 v[126:127], off
	v_lshl_add_u64 v[126:127], v[160:161], 0, s[22:23]
	s_mov_b32 m0, s65
	s_add_i32 s46, s76, s54
	global_load_lds_dwordx4 v[126:127], off
	v_lshl_add_u64 v[126:127], v[162:163], 0, s[22:23]
	s_mov_b32 m0, s46
	s_nop 0
	global_load_lds_dwordx4 v[126:127], off
	v_lshl_add_u64 v[126:127], v[164:165], 0, s[22:23]
	s_add_i32 m0, s46, 0x2000
	s_nop 0
	global_load_lds_dwordx4 v[126:127], off
	s_barrier
	s_setprio 1
	s_waitcnt lgkmcnt(7)
	v_mfma_f32_16x16x32_f16 v[92:95], v[44:47], v[80:83], v[92:95]
	v_mfma_f32_16x16x32_f16 v[88:91], v[60:63], v[80:83], v[88:91]
	s_waitcnt lgkmcnt(5)
	v_mfma_f32_16x16x32_f16 v[76:79], v[44:47], v[136:139], v[76:79]
	v_mfma_f32_16x16x32_f16 v[72:75], v[60:63], v[136:139], v[72:75]
	s_waitcnt lgkmcnt(3)
	v_mfma_f32_16x16x32_f16 v[28:31], v[44:47], v[144:147], v[28:31]
	v_mfma_f32_16x16x32_f16 v[24:27], v[60:63], v[144:147], v[24:27]
	s_waitcnt lgkmcnt(1)
	v_mfma_f32_16x16x32_f16 v[12:15], v[44:47], v[152:155], v[12:15]
	v_mfma_f32_16x16x32_f16 v[8:11], v[60:63], v[152:155], v[8:11]
	v_mfma_f32_16x16x32_f16 v[92:95], v[56:59], v[96:99], v[92:95]
	v_mfma_f32_16x16x32_f16 v[88:91], v[64:67], v[96:99], v[88:91]
	v_mfma_f32_16x16x32_f16 v[76:79], v[56:59], v[140:143], v[76:79]
	v_mfma_f32_16x16x32_f16 v[72:75], v[64:67], v[140:143], v[72:75]
	v_mfma_f32_16x16x32_f16 v[28:31], v[56:59], v[148:151], v[28:31]
	v_mfma_f32_16x16x32_f16 v[24:27], v[64:67], v[148:151], v[24:27]
	s_waitcnt lgkmcnt(0)
	v_mfma_f32_16x16x32_f16 v[12:15], v[56:59], v[156:159], v[12:15]
	v_mfma_f32_16x16x32_f16 v[8:11], v[64:67], v[156:159], v[8:11]
	s_setprio 0
	s_barrier
	s_add_i32 s46, s48, s54
	v_lshl_add_u64 v[126:127], v[166:167], 0, s[22:23]
	s_mov_b32 m0, s46
	ds_read_b128 v[44:47], v134
	ds_read_b128 v[56:59], v134 offset:1024
	ds_read_b128 v[60:63], v134 offset:2048
	ds_read_b128 v[64:67], v134 offset:3072
	global_load_lds_dwordx4 v[126:127], off
	v_lshl_add_u64 v[126:127], v[168:169], 0, s[22:23]
	s_add_i32 m0, s46, 0x2000
	s_nop 0
	global_load_lds_dwordx4 v[126:127], off
	s_waitcnt vmcnt(6)
	s_barrier
	s_setprio 1
	s_waitcnt lgkmcnt(3)
	v_mfma_f32_16x16x32_f16 v[84:87], v[44:47], v[80:83], v[84:87]
	s_waitcnt lgkmcnt(1)
	v_mfma_f32_16x16x32_f16 v[68:71], v[60:63], v[80:83], v[68:71]
	v_mfma_f32_16x16x32_f16 v[52:55], v[44:47], v[136:139], v[52:55]
	v_mfma_f32_16x16x32_f16 v[48:51], v[60:63], v[136:139], v[48:51]
	v_mfma_f32_16x16x32_f16 v[20:23], v[44:47], v[144:147], v[20:23]
	v_mfma_f32_16x16x32_f16 v[16:19], v[60:63], v[144:147], v[16:19]
	v_mfma_f32_16x16x32_f16 v[4:7], v[44:47], v[152:155], v[4:7]
	v_mfma_f32_16x16x32_f16 v[0:3], v[60:63], v[152:155], v[0:3]
	v_mfma_f32_16x16x32_f16 v[84:87], v[56:59], v[96:99], v[84:87]
	s_waitcnt lgkmcnt(0)
	v_mfma_f32_16x16x32_f16 v[80:83], v[64:67], v[96:99], v[68:71]
	v_mfma_f32_16x16x32_f16 v[52:55], v[56:59], v[140:143], v[52:55]
	v_mfma_f32_16x16x32_f16 v[48:51], v[64:67], v[140:143], v[48:51]
	v_mfma_f32_16x16x32_f16 v[20:23], v[56:59], v[148:151], v[20:23]
	v_mfma_f32_16x16x32_f16 v[16:19], v[64:67], v[148:151], v[16:19]
	v_mfma_f32_16x16x32_f16 v[4:7], v[56:59], v[156:159], v[4:7]
	v_mfma_f32_16x16x32_f16 v[0:3], v[64:67], v[156:159], v[0:3]
	s_setprio 0
	s_add_i32 s75, s75, 3
	s_add_u32 s44, s44, 0x180
	s_addc_u32 s45, s45, 0
	s_cmp_ge_i32 s75, s66
	s_cbranch_scc1 .Lrot_exit_mlp1
	s_add_u32 s46, s40, s44
	s_addc_u32 s47, s41, s45
	s_add_u32 s46, s46, 0x180
	s_addc_u32 s47, s47, 0
	s_add_u32 s48, s42, s44
	s_addc_u32 s49, s43, s45
	s_add_u32 s76, s48, 0x180
	s_addc_u32 s77, s49, 0
	s_cmp_eq_u32 s67, s75
	s_cselect_b32 s49, s7, s47
	s_cselect_b32 s48, s6, s46
	s_cselect_b32 s47, s5, s77
	s_cselect_b32 s46, s4, s76
	s_add_i32 s76, s19, s54
	v_lshl_add_u64 v[126:127], v[32:33], 0, s[44:45]
	s_barrier
	s_branch .LBB5_55

.LBB6_22:
	s_mov_b32 m0, s68
	ds_read_b128 v[132:135], v131 offset:16384
	ds_read_b128 v[136:139], v131 offset:17408
	ds_read_b128 v[140:143], v131 offset:18432
	ds_read_b128 v[144:147], v131 offset:19456
	ds_read_b128 v[148:151], v182
	ds_read_b128 v[152:155], v182 offset:1024
	ds_read_b128 v[156:159], v182 offset:2048
	ds_read_b128 v[160:163], v182 offset:3072
	ds_read_b128 v[164:167], v182 offset:4096
	ds_read_b128 v[168:171], v182 offset:5120
	ds_read_b128 v[172:175], v182 offset:6144
	ds_read_b128 v[176:179], v182 offset:7168
	global_load_lds_dwordx4 v[180:181], off
	v_lshl_add_u64 v[180:181], v[118:119], 0, s[28:29]
	s_add_i32 m0, s68, 0x2000
	s_nop 0
	global_load_lds_dwordx4 v[180:181], off
	s_barrier
	s_setprio 1
	s_waitcnt lgkmcnt(7)
	v_mfma_f32_16x16x32_f16 v[40:43], v[132:135], v[148:151], v[40:43]
	v_mfma_f32_16x16x32_f16 v[44:47], v[140:143], v[148:151], v[44:47]
	s_waitcnt lgkmcnt(5)
	v_mfma_f32_16x16x32_f16 v[32:35], v[132:135], v[156:159], v[32:35]
	v_mfma_f32_16x16x32_f16 v[28:31], v[140:143], v[156:159], v[28:31]
	s_waitcnt lgkmcnt(3)
	v_mfma_f32_16x16x32_f16 v[20:23], v[132:135], v[164:167], v[20:23]
	v_mfma_f32_16x16x32_f16 v[16:19], v[140:143], v[164:167], v[16:19]
	s_waitcnt lgkmcnt(1)
	v_mfma_f32_16x16x32_f16 v[8:11], v[132:135], v[172:175], v[8:11]
	v_mfma_f32_16x16x32_f16 v[4:7], v[140:143], v[172:175], v[4:7]
	v_mfma_f32_16x16x32_f16 v[40:43], v[136:139], v[152:155], v[40:43]
	v_mfma_f32_16x16x32_f16 v[44:47], v[144:147], v[152:155], v[44:47]
	v_mfma_f32_16x16x32_f16 v[32:35], v[136:139], v[160:163], v[32:35]
	v_mfma_f32_16x16x32_f16 v[28:31], v[144:147], v[160:163], v[28:31]
	v_mfma_f32_16x16x32_f16 v[20:23], v[136:139], v[168:171], v[20:23]
	v_mfma_f32_16x16x32_f16 v[16:19], v[144:147], v[168:171], v[16:19]
	s_waitcnt lgkmcnt(0)
	v_mfma_f32_16x16x32_f16 v[8:11], v[136:139], v[176:179], v[8:11]
	v_mfma_f32_16x16x32_f16 v[4:7], v[144:147], v[176:179], v[4:7]
	s_setprio 0
	s_barrier
	v_lshl_add_u64 v[140:141], v[120:121], 0, s[28:29]
	s_add_i32 m0, s47, 0x18000
	ds_read_b128 v[132:135], v131 offset:20480
	ds_read_b128 v[136:139], v131 offset:21504
	global_load_lds_dwordx4 v[140:141], off
	v_lshl_add_u64 v[140:141], v[122:123], 0, s[28:29]
	s_add_i32 m0, s47, 0x1a000
	s_nop 0
	global_load_lds_dwordx4 v[140:141], off
	v_lshl_add_u64 v[140:141], v[124:125], 0, s[28:29]
	s_add_i32 m0, s47, 0x1c000
	s_nop 0
	global_load_lds_dwordx4 v[140:141], off
	s_cmp_lg_u32 s65, 0
	s_cbranch_scc1 .Lm2_norm_0
	s_mul_i32 s70, s58, 0xc0
	v_add_u32_e32 v234, s70, v129
	v_ashrrev_i32_e32 v235, 31, v234
	v_lshlrev_b64 v[234:235], 2, v[234:235]
	v_lshl_add_u64 v[234:235], s[18:19], 0, v[234:235]
	global_load_dwordx4 v[222:225], v[234:235], off
	global_load_dwordx4 v[226:229], v[234:235], off offset:64
	global_load_dwordx4 v[230:233], v[234:235], off offset:128
	global_load_dwordx2 v[198:199], v[190:191], off
	global_load_dwordx2 v[200:201], v[190:191], off offset:32
	global_load_dwordx2 v[202:203], v[190:191], off offset:64
	global_load_dwordx2 v[204:205], v[192:193], off
	s_waitcnt vmcnt(12)
	s_branch .Lm2_join_0

.Lm2_join_2:
	s_barrier
	s_setprio 1
	s_waitcnt lgkmcnt(1)
	v_mfma_f32_16x16x32_f16 v[36:39], v[132:135], v[148:151], v[36:39]
	v_mfma_f32_16x16x32_f16 v[24:27], v[132:135], v[156:159], v[24:27]
	v_mfma_f32_16x16x32_f16 v[12:15], v[132:135], v[164:167], v[12:15]
	v_mfma_f32_16x16x32_f16 v[0:3], v[132:135], v[172:175], v[0:3]
	s_waitcnt lgkmcnt(0)
	v_mfma_f32_16x16x32_f16 v[36:39], v[136:139], v[152:155], v[36:39]
	v_mfma_f32_16x16x32_f16 v[24:27], v[136:139], v[160:163], v[24:27]
	v_mfma_f32_16x16x32_f16 v[12:15], v[136:139], v[168:171], v[12:15]
	v_mfma_f32_16x16x32_f16 v[0:3], v[136:139], v[176:179], v[0:3]
	s_setprio 0
	s_add_i32 s65, s65, 3
	s_add_u32 s28, s28, 0x180
	s_addc_u32 s29, s29, 0
	s_cmp_ge_i32 s65, s59
	s_cbranch_scc1 .Lrot_exit_mlp2
	s_add_u32 s30, s22, s28
	s_addc_u32 s31, s23, s29
	s_add_u32 s30, s30, 0x180
	s_addc_u32 s31, s31, 0
	s_add_u32 s66, s24, s28
	s_addc_u32 s67, s25, s29
	s_add_u32 s68, s66, 0x180
	s_addc_u32 s69, s67, 0
	s_cmp_eq_u32 s60, s65
	s_cselect_b32 s67, s27, s31
	s_cselect_b32 s66, s26, s30
	s_cselect_b32 s31, s5, s69
	s_cselect_b32 s30, s4, s68
	s_add_i32 s68, s62, s42
	v_add_u32_e32 v131, 0, v128
	v_add_u32_e32 v182, 0, v127
	v_lshl_add_u64 v[180:181], v[116:117], 0, s[28:29]
	s_barrier
	s_branch .LBB6_22
